# v47 + weight-side LDS-DMA loads of the two MoE GEMM K-loops marked nt (streamed once per XCD) so the re-used activation slabs stay in L2
# baseline (speedup 1.0000x reference)
; #define PG8_STAGE(bufoff, gbase, voff) do { _Pragma("unroll") for (int _i = 0; _i < 2; ++_i) \
;         __builtin_amdgcn_global_load_lds((const unsigned*)((const char*)(gbase) + (voff)[_i]), (PG8_LAS unsigned*)(lds + (bufoff) + ldsw + _i * 8192), 16, 0, 0); } while (0)
; #define PG8_LDA(dst, b, h) do { _Pragma("unroll") for (int m = 0; m < 4; ++m) _Pragma("unroll") for (int k = 0; k < 2; ++k) dst[m][k] = *(const PG8_LAS bf16x8*)(lds + PG8_SA(b, h) + aoff + m * 2048 + k * 1024); } while (0)
; #define PG8_LDB(dst, b, h) do { _Pragma("unroll") for (int n = 0; n < 2; ++n) _Pragma("unroll") for (int k = 0; k < 2; ++k) dst[n][k] = *(const PG8_LAS bf16x8*)(lds + PG8_SB(b, h) + boff + n * 2048 + k * 1024); } while (0)
; #define PG8_WAIT_V(n) asm volatile("s_waitcnt vmcnt(" #n ")" ::: "memory")
; #define PG8_WAIT_L(n) asm volatile("s_waitcnt lgkmcnt(" #n ")" ::: "memory")
; #define PG8_BAR __builtin_amdgcn_s_barrier()
; #define PG8_SCHED __builtin_amdgcn_sched_barrier(0)
; #define PG8_WAIT_V(n) asm volatile("s_waitcnt vmcnt(" #n ")" ::: "memory")
; template <class Epi, class Sched, int SCW, int SCX, int SCW1 = SCW>
; __device__ __forceinline__ void gemm_phase_f8(PG8_LAS unsigned char* lds, const Gemm g, const Sched& S, const Epi& E, const int tid) {
;     ...
;         const char* nA = has_next ? (const char*)g.A + (size_t)nxt.pm * tstep + (size_t)nxt.k0 : cA; const char* nB = has_next ? (const char*)g.Bt + (size_t)nxt.pn * tstep + (size_t)nxt.k0 * 256 : cB;
;         for (int t = 0; t < nt; t += 2) {
;             const bool last = (t == nt - 2);
;             const char* a1 = cA + (size_t)(t + 1) * kstep;
;             const char* a2 = last ? nA : cA + (size_t)(t + 2) * kstep; const char* b2 = last ? nB : cB + (size_t)(t + 2) * kstepB;
;             const char* a3 = a2 + kstep; const char* b3 = b2 + kstepB;
;             if (last && has_next) S.a_ready(nxt);
;             PG8_LDB(B0, 0, 0); PG8_LDB(B1, 0, 1); PG8_SCHED; PG8_LDA(At, 0, 0); PG8_STAGE(PG8_SA(1, 1), a1 + hstep, voffA);
;             PG8_WAIT_V(8); PG8_WAIT_L(0); PG8_BAR; PG8_MMA(0, 0, At, B0); PG8_MMA(0, 1, At, B1); PG8_BAR; PG8_SCHED;
;             PG8_LDA(At, 0, 1); PG8_STAGE(PG8_SB(0, 0), b2, voffB); PG8_STAGE(PG8_SB(0, 1), b2 + hstepB, voffB); PG8_STAGE(PG8_SA(0, 0), a2, voffA);
;             PG8_WAIT_V(8); PG8_WAIT_L(0); PG8_BAR; PG8_MMA(1, 0, At, B0); PG8_MMA(1, 1, At, B1); PG8_BAR; PG8_SCHED;
.LBB0_1896:
	s_add_u32 s6, s40, 0xfffc0080
	s_addc_u32 s7, s41, -1
	s_add_i32 s67, 0, 0x10000
	s_cmp_eq_u32 s66, 12
	v_add_u32_e32 v144, s67, v131
	s_cselect_b32 s43, s15, s7
	s_cselect_b32 s42, s63, s6
	v_add_u32_e32 v145, s67, v150
	ds_read_b128 v[160:163], v144
	ds_read_b128 v[164:167], v145
	v_add_u32_e32 v144, s67, v151
	s_cselect_b32 s7, s17, s65
	s_cselect_b32 s6, s21, s64
	s_add_i32 s70, 0, 0x14000
	v_add_u32_e32 v145, s67, v152
	ds_read_b128 v[168:171], v144
	ds_read_b128 v[172:175], v145
	v_add_u32_e32 v144, s70, v131
	v_add_u32_e32 v145, s70, v150
	ds_read_b128 v[176:179], v144
	ds_read_b128 v[180:183], v145
	v_add_u32_e32 v144, s70, v151
	v_add_u32_e32 v145, s70, v152
	ds_read_b128 v[184:187], v144
	ds_read_b128 v[188:191], v145
	v_lshl_add_u64 v[144:145], s[40:41], 0, v[140:141]
	s_add_i32 m0, s31, 0xc000
	ds_read_b128 v[198:201], v155
	ds_read_b128 v[206:209], v155 offset:4096
	ds_read_b128 v[202:205], v156
	ds_read_b128 v[210:213], v156 offset:4096
	ds_read_b128 v[214:217], v157
	ds_read_b128 v[222:225], v157 offset:4096
	ds_read_b128 v[218:221], v158
	ds_read_b128 v[226:229], v158 offset:4096
	global_load_lds_dwordx4 v[144:145], off
	v_lshl_add_u64 v[144:145], s[40:41], 0, v[142:143]
	s_add_i32 m0, s31, 0xe000
	s_nop 0
	global_load_lds_dwordx4 v[144:145], off
	s_waitcnt vmcnt(8)
	s_waitcnt lgkmcnt(0)
	s_barrier
	s_setprio 1
	s_waitcnt lgkmcnt(0)
	v_mfma_scale_f32_32x32x64_f8f6f4 v[98:113], v[160:167], v[198:205], v[98:113], v233, v232 op_sel_hi:[0,0,0]
	v_mfma_scale_f32_32x32x64_f8f6f4 v[66:81], v[160:167], v[206:213], v[66:81], v233, v232 op_sel_hi:[0,0,0]
	v_mfma_scale_f32_32x32x64_f8f6f4 v[98:113], v[168:175], v[214:221], v[98:113], v233, v232 op_sel_hi:[0,0,0]
	v_mfma_scale_f32_32x32x64_f8f6f4 v[66:81], v[168:175], v[222:229], v[66:81], v233, v232 op_sel_hi:[0,0,0]
	s_setprio 0
	s_setprio 1
	v_mfma_scale_f32_32x32x64_f8f6f4 v[114:129], v[176:183], v[198:205], v[114:129], v232, v232 op_sel_hi:[0,0,0]
	v_mfma_scale_f32_32x32x64_f8f6f4 v[82:97], v[176:183], v[206:213], v[82:97], v232, v232 op_sel_hi:[0,0,0]
	v_mfma_scale_f32_32x32x64_f8f6f4 v[114:129], v[184:191], v[214:221], v[114:129], v232, v232 op_sel_hi:[0,0,0]
	v_mfma_scale_f32_32x32x64_f8f6f4 v[82:97], v[184:191], v[222:229], v[82:97], v232, v232 op_sel_hi:[0,0,0]
	s_setprio 0
	s_barrier
	s_add_i32 s67, s67, s48
	v_lshl_add_u64 v[144:145], s[6:7], 0, v[136:137]
	s_mov_b32 m0, s67
	ds_read_b128 v[198:201], v155 offset:16384
	ds_read_b128 v[206:209], v155 offset:20480
	ds_read_b128 v[202:205], v156 offset:16384
	ds_read_b128 v[210:213], v156 offset:20480
	ds_read_b128 v[214:217], v157 offset:16384
	ds_read_b128 v[222:225], v157 offset:20480
	ds_read_b128 v[218:221], v158 offset:16384
	ds_read_b128 v[226:229], v158 offset:20480
	global_load_lds_dwordx4 v[144:145], off nt
	s_add_i32 m0, s67, 0x2000
	s_add_u32 s68, s6, 0x4000
	v_lshl_add_u64 v[144:145], s[6:7], 0, v[132:133]
	s_addc_u32 s69, s7, 0
	s_add_i32 s67, s70, s48
	global_load_lds_dwordx4 v[144:145], off nt
	v_lshl_add_u64 v[144:145], s[68:69], 0, v[136:137]
	s_mov_b32 m0, s67
	v_lshl_add_u64 v[146:147], s[42:43], 0, v[134:135]
	global_load_lds_dwordx4 v[144:145], off nt
	v_lshl_add_u64 v[144:145], s[68:69], 0, v[132:133]
	s_add_i32 m0, s67, 0x2000
	s_nop 0
	global_load_lds_dwordx4 v[144:145], off nt
	v_lshl_add_u64 v[144:145], s[42:43], 0, v[138:139]
	s_mov_b32 m0, s31
	s_nop 0
	global_load_lds_dwordx4 v[144:145], off
	s_mov_b32 m0, s39
	s_nop 0
	global_load_lds_dwordx4 v[146:147], off
	s_waitcnt vmcnt(8)
	s_waitcnt lgkmcnt(0)
	s_barrier
	s_setprio 1
	s_waitcnt lgkmcnt(0)
	v_mfma_scale_f32_32x32x64_f8f6f4 v[34:49], v[160:167], v[198:205], v[34:49], v233, v232 op_sel_hi:[0,0,0]
	v_mfma_scale_f32_32x32x64_f8f6f4 v[2:17], v[160:167], v[206:213], v[2:17], v233, v232 op_sel_hi:[0,0,0]
	v_mfma_scale_f32_32x32x64_f8f6f4 v[34:49], v[168:175], v[214:221], v[34:49], v233, v232 op_sel_hi:[0,0,0]
	v_mfma_scale_f32_32x32x64_f8f6f4 v[2:17], v[168:175], v[222:229], v[2:17], v233, v232 op_sel_hi:[0,0,0]
	s_setprio 0
	s_setprio 1
	v_mfma_scale_f32_32x32x64_f8f6f4 v[50:65], v[176:183], v[198:205], v[50:65], v232, v232 op_sel_hi:[0,0,0]
	v_mfma_scale_f32_32x32x64_f8f6f4 v[18:33], v[176:183], v[206:213], v[18:33], v232, v232 op_sel_hi:[0,0,0]
	v_mfma_scale_f32_32x32x64_f8f6f4 v[50:65], v[184:191], v[214:221], v[50:65], v232, v232 op_sel_hi:[0,0,0]
	v_mfma_scale_f32_32x32x64_f8f6f4 v[18:33], v[184:191], v[222:229], v[18:33], v232, v232 op_sel_hi:[0,0,0]
	s_setprio 0
	s_barrier
; #define PG8_STAGE(bufoff, gbase, voff) do { _Pragma("unroll") for (int _i = 0; _i < 2; ++_i) \
;         __builtin_amdgcn_global_load_lds((const unsigned*)((const char*)(gbase) + (voff)[_i]), (PG8_LAS unsigned*)(lds + (bufoff) + ldsw + _i * 8192), 16, 0, 0); } while (0)
; #define PG8_LDA(dst, b, h) do { _Pragma("unroll") for (int m = 0; m < 4; ++m) _Pragma("unroll") for (int k = 0; k < 2; ++k) dst[m][k] = *(const PG8_LAS bf16x8*)(lds + PG8_SA(b, h) + aoff + m * 2048 + k * 1024); } while (0)
; #define PG8_LDB(dst, b, h) do { _Pragma("unroll") for (int n = 0; n < 2; ++n) _Pragma("unroll") for (int k = 0; k < 2; ++k) dst[n][k] = *(const PG8_LAS bf16x8*)(lds + PG8_SB(b, h) + boff + n * 2048 + k * 1024); } while (0)
; #define PG8_MMA(ai, bj, At, Bt) do { __builtin_amdgcn_s_setprio(1); _Pragma("unroll") for (int m = 0; m < 4; ++m) _Pragma("unroll") for (int n = 0; n < 2; ++n) _Pragma("unroll") for (int k = 0; k < 2; ++k) \
;         acc[ai][bj][m][n] = __builtin_amdgcn_mfma_f32_16x16x32_bf16(Bt[n][k], At[m][k], acc[ai][bj][m][n], 0, 0, 0); __builtin_amdgcn_s_setprio(0); } while (0)
; #define PG8_WAIT_V(n) asm volatile("s_waitcnt vmcnt(" #n ")" ::: "memory")
; #define PG8_WAIT_L(n) asm volatile("s_waitcnt lgkmcnt(" #n ")" ::: "memory")
; #define PG8_BAR __builtin_amdgcn_s_barrier()
; #define PG8_SCHED __builtin_amdgcn_sched_barrier(0)
; #define PG8_STAGE(bufoff, gbase, voff) do { _Pragma("unroll") for (int _i = 0; _i < 2; ++_i) \
;         __builtin_amdgcn_global_load_lds((const unsigned*)((const char*)(gbase) + (voff)[_i]), (PG8_LAS unsigned*)(lds + (bufoff) + ldsw + _i * 8192), 16, 0, 0); } while (0)
; template <class Epi, class Sched, int SCW, int SCX, int SCW1 = SCW>
; __device__ __forceinline__ void gemm_phase_f8(PG8_LAS unsigned char* lds, const Gemm g, const Sched& S, const Epi& E, const int tid) {
;     ...
;             PG8_LDB(B0, 1, 0); PG8_LDB(B1, 1, 1); PG8_SCHED; PG8_LDA(At, 1, 0); PG8_STAGE(PG8_SA(0, 1), a2 + hstep, voffA);
;             PG8_WAIT_V(8); PG8_WAIT_L(0); PG8_BAR; PG8_MMA(0, 0, At, B0); PG8_MMA(0, 1, At, B1); PG8_BAR; PG8_SCHED;
;             PG8_LDA(At, 1, 1); PG8_STAGE(PG8_SB(1, 0), b3, voffB); PG8_STAGE(PG8_SB(1, 1), b3 + hstepB, voffB); PG8_STAGE(PG8_SA(1, 0), a3, voffA);
;             PG8_WAIT_V(8); PG8_WAIT_L(0); PG8_BAR; PG8_MMA(1, 0, At, B0); PG8_MMA(1, 1, At, B1); PG8_BAR; PG8_SCHED;
;         }
	s_add_i32 s67, 0, 0x18000
	v_add_u32_e32 v148, s67, v131
	v_add_u32_e32 v149, s67, v150
	ds_read_b128 v[160:163], v148
	ds_read_b128 v[164:167], v149
	v_add_u32_e32 v148, s67, v151
	s_add_i32 s68, 0, 0x1c000
	v_add_u32_e32 v149, s67, v152
	ds_read_b128 v[168:171], v148
	ds_read_b128 v[172:175], v149
	v_add_u32_e32 v148, s68, v131
	v_add_u32_e32 v149, s68, v150
	ds_read_b128 v[176:179], v148
	ds_read_b128 v[180:183], v149
	v_add_u32_e32 v148, s68, v151
	v_add_u32_e32 v149, s68, v152
	ds_read_b128 v[184:187], v148
	ds_read_b128 v[188:191], v149
	s_add_u32 s42, s42, 0x40000
	s_addc_u32 s43, s43, 0
	s_mov_b32 m0, s57
	v_lshl_add_u64 v[148:149], s[42:43], 0, v[138:139]
	ds_read_b128 v[198:201], v155 offset:32768
	ds_read_b128 v[206:209], v155 offset:36864
	ds_read_b128 v[202:205], v156 offset:32768
	ds_read_b128 v[210:213], v156 offset:36864
	ds_read_b128 v[214:217], v157 offset:32768
	ds_read_b128 v[222:225], v157 offset:36864
	ds_read_b128 v[218:221], v158 offset:32768
	ds_read_b128 v[226:229], v158 offset:36864
	global_load_lds_dwordx4 v[148:149], off
	v_lshl_add_u64 v[148:149], s[42:43], 0, v[134:135]
	s_mov_b32 m0, s58
	s_nop 0
	global_load_lds_dwordx4 v[148:149], off
	s_waitcnt vmcnt(8)
	s_waitcnt lgkmcnt(0)
	s_barrier
	s_setprio 1
	s_waitcnt lgkmcnt(0)
	v_mfma_scale_f32_32x32x64_f8f6f4 v[98:113], v[160:167], v[198:205], v[98:113], v233, v232 op_sel_hi:[0,0,0]
	v_mfma_scale_f32_32x32x64_f8f6f4 v[66:81], v[160:167], v[206:213], v[66:81], v233, v232 op_sel_hi:[0,0,0]
	v_mfma_scale_f32_32x32x64_f8f6f4 v[98:113], v[168:175], v[214:221], v[98:113], v233, v232 op_sel_hi:[0,0,0]
	v_mfma_scale_f32_32x32x64_f8f6f4 v[66:81], v[168:175], v[222:229], v[66:81], v233, v232 op_sel_hi:[0,0,0]
	s_setprio 0
	s_setprio 1
	v_mfma_scale_f32_32x32x64_f8f6f4 v[114:129], v[176:183], v[198:205], v[114:129], v232, v232 op_sel_hi:[0,0,0]
	v_mfma_scale_f32_32x32x64_f8f6f4 v[82:97], v[176:183], v[206:213], v[82:97], v232, v232 op_sel_hi:[0,0,0]
	v_mfma_scale_f32_32x32x64_f8f6f4 v[114:129], v[184:191], v[214:221], v[114:129], v232, v232 op_sel_hi:[0,0,0]
	v_mfma_scale_f32_32x32x64_f8f6f4 v[82:97], v[184:191], v[222:229], v[82:97], v232, v232 op_sel_hi:[0,0,0]
	s_setprio 0
	s_barrier
	s_add_u32 s42, s6, 0x8000
	s_addc_u32 s43, s7, 0
	s_add_i32 s67, s67, s48
	v_lshl_add_u64 v[148:149], s[42:43], 0, v[136:137]
	s_mov_b32 m0, s67
	ds_read_b128 v[198:201], v155 offset:49152
	ds_read_b128 v[206:209], v155 offset:53248
	ds_read_b128 v[202:205], v156 offset:49152
	ds_read_b128 v[210:213], v156 offset:53248
	ds_read_b128 v[214:217], v157 offset:49152
	ds_read_b128 v[222:225], v157 offset:53248
	ds_read_b128 v[218:221], v158 offset:49152
	ds_read_b128 v[226:229], v158 offset:53248
	global_load_lds_dwordx4 v[148:149], off nt
	s_add_i32 m0, s67, 0x2000
	s_add_u32 s6, s6, 0xc000
	v_lshl_add_u64 v[148:149], s[42:43], 0, v[132:133]
	s_addc_u32 s7, s7, 0
	s_add_i32 s42, s68, s48
	global_load_lds_dwordx4 v[148:149], off nt
	v_lshl_add_u64 v[148:149], s[6:7], 0, v[136:137]
	s_mov_b32 m0, s42
	v_lshl_add_u64 v[144:145], v[144:145], 0, s[34:35]
	global_load_lds_dwordx4 v[148:149], off nt
	v_lshl_add_u64 v[148:149], s[6:7], 0, v[132:133]
	s_add_i32 m0, s42, 0x2000
	s_nop 0
	global_load_lds_dwordx4 v[148:149], off nt
	s_mov_b32 m0, s59
	s_nop 0
	global_load_lds_dwordx4 v[144:145], off
	v_lshl_add_u64 v[144:145], v[146:147], 0, s[34:35]
	s_mov_b32 m0, s60
	s_nop 0
	global_load_lds_dwordx4 v[144:145], off
	s_waitcnt vmcnt(8)
	s_waitcnt lgkmcnt(0)
	s_barrier
	s_setprio 1
	s_waitcnt lgkmcnt(0)
	v_mfma_scale_f32_32x32x64_f8f6f4 v[34:49], v[160:167], v[198:205], v[34:49], v233, v232 op_sel_hi:[0,0,0]
	v_mfma_scale_f32_32x32x64_f8f6f4 v[2:17], v[160:167], v[206:213], v[2:17], v233, v232 op_sel_hi:[0,0,0]
	v_mfma_scale_f32_32x32x64_f8f6f4 v[34:49], v[168:175], v[214:221], v[34:49], v233, v232 op_sel_hi:[0,0,0]
	v_mfma_scale_f32_32x32x64_f8f6f4 v[2:17], v[168:175], v[222:229], v[2:17], v233, v232 op_sel_hi:[0,0,0]
	s_setprio 0
	s_setprio 1
	v_mfma_scale_f32_32x32x64_f8f6f4 v[50:65], v[176:183], v[198:205], v[50:65], v232, v232 op_sel_hi:[0,0,0]
	v_mfma_scale_f32_32x32x64_f8f6f4 v[18:33], v[176:183], v[206:213], v[18:33], v232, v232 op_sel_hi:[0,0,0]
	v_mfma_scale_f32_32x32x64_f8f6f4 v[50:65], v[184:191], v[214:221], v[50:65], v232, v232 op_sel_hi:[0,0,0]
	v_mfma_scale_f32_32x32x64_f8f6f4 v[18:33], v[184:191], v[222:229], v[18:33], v232, v232 op_sel_hi:[0,0,0]
	s_setprio 0
	s_barrier
	s_add_i32 s66, s66, 2
	s_add_u32 s64, s64, 0x10000
	s_addc_u32 s65, s65, 0
	s_add_u32 s40, s40, 0x100
	s_addc_u32 s41, s41, 0
	s_cmp_gt_u32 s66, 13
	s_cbranch_scc0 .LBB0_1896
	s_and_b64 vcc, exec, s[8:9]
	s_cbranch_vccz .LBB0_1899
	s_barrier

; #define PG8_STAGE(bufoff, gbase, voff) do { _Pragma("unroll") for (int _i = 0; _i < 2; ++_i) \
;         __builtin_amdgcn_global_load_lds((const unsigned*)((const char*)(gbase) + (voff)[_i]), (PG8_LAS unsigned*)(lds + (bufoff) + ldsw + _i * 8192), 16, 0, 0); } while (0)
; #define PG8_LDA(dst, b, h) do { _Pragma("unroll") for (int m = 0; m < 4; ++m) _Pragma("unroll") for (int k = 0; k < 2; ++k) dst[m][k] = *(const PG8_LAS bf16x8*)(lds + PG8_SA(b, h) + aoff + m * 2048 + k * 1024); } while (0)
; #define PG8_LDB(dst, b, h) do { _Pragma("unroll") for (int n = 0; n < 2; ++n) _Pragma("unroll") for (int k = 0; k < 2; ++k) dst[n][k] = *(const PG8_LAS bf16x8*)(lds + PG8_SB(b, h) + boff + n * 2048 + k * 1024); } while (0)
; #define PG8_WAIT_V(n) asm volatile("s_waitcnt vmcnt(" #n ")" ::: "memory")
; #define PG8_WAIT_L(n) asm volatile("s_waitcnt lgkmcnt(" #n ")" ::: "memory")
; #define PG8_BAR __builtin_amdgcn_s_barrier()
; #define PG8_SCHED __builtin_amdgcn_sched_barrier(0)
; #define PG8_WAIT_V(n) asm volatile("s_waitcnt vmcnt(" #n ")" ::: "memory")
; template <class Epi, class Sched, int SCW, int SCX, int SCW1 = SCW>
; __device__ __forceinline__ void gemm_phase_f8(PG8_LAS unsigned char* lds, const Gemm g, const Sched& S, const Epi& E, const int tid) {
;     ...
;         const char* nA = has_next ? (const char*)g.A + (size_t)nxt.pm * tstep + (size_t)nxt.k0 : cA; const char* nB = has_next ? (const char*)g.Bt + (size_t)nxt.pn * tstep + (size_t)nxt.k0 * 256 : cB;
;         for (int t = 0; t < nt; t += 2) {
;             const bool last = (t == nt - 2);
;             const char* a1 = cA + (size_t)(t + 1) * kstep;
;             const char* a2 = last ? nA : cA + (size_t)(t + 2) * kstep; const char* b2 = last ? nB : cB + (size_t)(t + 2) * kstepB;
;             const char* a3 = a2 + kstep; const char* b3 = b2 + kstepB;
;             if (last && has_next) S.a_ready(nxt);
;             PG8_LDB(B0, 0, 0); PG8_LDB(B1, 0, 1); PG8_SCHED; PG8_LDA(At, 0, 0); PG8_STAGE(PG8_SA(1, 1), a1 + hstep, voffA);
;             PG8_WAIT_V(8); PG8_WAIT_L(0); PG8_BAR; PG8_MMA(0, 0, At, B0); PG8_MMA(0, 1, At, B1); PG8_BAR; PG8_SCHED;
;             PG8_LDA(At, 0, 1); PG8_STAGE(PG8_SB(0, 0), b2, voffB); PG8_STAGE(PG8_SB(0, 1), b2 + hstepB, voffB); PG8_STAGE(PG8_SA(0, 0), a2, voffA);
;             PG8_WAIT_V(8); PG8_WAIT_L(0); PG8_BAR; PG8_MMA(1, 0, At, B0); PG8_MMA(1, 1, At, B1); PG8_BAR; PG8_SCHED;
.LBB0_2000:
	s_add_i32 s63, s6, 2
	s_add_u32 s7, s28, 0x4000
	s_addc_u32 s30, s29, 0
	s_add_i32 s66, 0, 0x10000
	s_cmp_eq_u32 s12, s6
	v_add_u32_e32 v153, s66, v131
	v_add_u32_e32 v158, s66, v144
	s_cselect_b32 s31, s21, s30
	s_cselect_b32 s30, s20, s7
	ds_read_b128 v[154:157], v153
	ds_read_b128 v[158:161], v158
	v_add_u32_e32 v153, s66, v145
	v_add_u32_e32 v166, s66, v146
	s_cselect_b32 s7, s23, s17
	s_cselect_b32 s6, s22, s13
	s_add_i32 s87, 0, 0x14000
	ds_read_b128 v[162:165], v153
	ds_read_b128 v[166:169], v166
	v_add_u32_e32 v153, s87, v131
	v_add_u32_e32 v174, s87, v144
	ds_read_b128 v[170:173], v153
	ds_read_b128 v[174:177], v174
	v_add_u32_e32 v153, s87, v145
	v_add_u32_e32 v182, s87, v146
	ds_read_b128 v[178:181], v153
	ds_read_b128 v[182:185], v182
	v_lshl_add_u64 v[194:195], s[28:29], 0, v[140:141]
	s_add_i32 m0, s51, 0xc000
	ds_read_b128 v[186:189], v149
	ds_read_b128 v[198:201], v149 offset:4096
	ds_read_b128 v[190:193], v150
	ds_read_b128 v[202:205], v150 offset:4096
	ds_read_b128 v[206:209], v151
	ds_read_b128 v[214:217], v151 offset:4096
	ds_read_b128 v[210:213], v152
	ds_read_b128 v[218:221], v152 offset:4096
	global_load_lds_dwordx4 v[194:195], off
	v_lshl_add_u64 v[194:195], s[28:29], 0, v[142:143]
	s_add_i32 m0, s51, 0xe000
	s_nop 0
	global_load_lds_dwordx4 v[194:195], off
	s_waitcnt vmcnt(8)
	s_waitcnt lgkmcnt(0)
	s_barrier
	s_setprio 1
	s_waitcnt lgkmcnt(0)
	v_mfma_scale_f32_32x32x64_f8f6f4 v[114:129], v[154:161], v[186:193], v[114:129], v233, v234 op_sel_hi:[0,0,0]
	v_mfma_scale_f32_32x32x64_f8f6f4 v[82:97], v[154:161], v[198:205], v[82:97], v233, v234 op_sel_hi:[0,0,0]
	v_mfma_scale_f32_32x32x64_f8f6f4 v[114:129], v[162:169], v[206:213], v[114:129], v233, v234 op_sel_hi:[0,0,0]
	v_mfma_scale_f32_32x32x64_f8f6f4 v[82:97], v[162:169], v[214:221], v[82:97], v233, v234 op_sel_hi:[0,0,0]
	s_setprio 0
	s_setprio 1
	v_mfma_scale_f32_32x32x64_f8f6f4 v[98:113], v[170:177], v[186:193], v[98:113], v233, v234 op_sel_hi:[0,0,0]
	v_mfma_scale_f32_32x32x64_f8f6f4 v[66:81], v[170:177], v[198:205], v[66:81], v233, v234 op_sel_hi:[0,0,0]
	v_mfma_scale_f32_32x32x64_f8f6f4 v[98:113], v[178:185], v[206:213], v[98:113], v233, v234 op_sel_hi:[0,0,0]
	v_mfma_scale_f32_32x32x64_f8f6f4 v[66:81], v[178:185], v[214:221], v[66:81], v233, v234 op_sel_hi:[0,0,0]
	s_setprio 0
	s_barrier
	s_add_i32 s66, s66, s50
	v_lshl_add_u64 v[194:195], s[6:7], 0, v[134:135]
	s_mov_b32 m0, s66
	ds_read_b128 v[186:189], v149 offset:16384
	ds_read_b128 v[198:201], v149 offset:20480
	ds_read_b128 v[190:193], v150 offset:16384
	ds_read_b128 v[202:205], v150 offset:20480
	ds_read_b128 v[206:209], v151 offset:16384
	ds_read_b128 v[214:217], v151 offset:20480
	ds_read_b128 v[210:213], v152 offset:16384
	ds_read_b128 v[218:221], v152 offset:20480
	global_load_lds_dwordx4 v[194:195], off nt
	s_add_i32 m0, s66, 0x2000
	s_add_u32 s88, s6, 0x4000
	v_lshl_add_u64 v[194:195], s[6:7], 0, v[138:139]
	s_addc_u32 s89, s7, 0
	s_add_i32 s66, s87, s50
	global_load_lds_dwordx4 v[194:195], off nt
	v_lshl_add_u64 v[194:195], s[88:89], 0, v[134:135]
	s_mov_b32 m0, s66
	v_lshl_add_u64 v[222:223], s[30:31], 0, v[136:137]
	global_load_lds_dwordx4 v[194:195], off nt
	v_lshl_add_u64 v[194:195], s[88:89], 0, v[138:139]
	s_add_i32 m0, s66, 0x2000
	s_nop 0
	global_load_lds_dwordx4 v[194:195], off nt
	v_lshl_add_u64 v[194:195], s[30:31], 0, v[132:133]
	s_mov_b32 m0, s51
	s_nop 0
	global_load_lds_dwordx4 v[194:195], off
	s_mov_b32 m0, s52
	s_nop 0
	global_load_lds_dwordx4 v[222:223], off
	s_waitcnt vmcnt(8)
	s_waitcnt lgkmcnt(0)
	s_barrier
	s_setprio 1
	s_waitcnt lgkmcnt(0)
	v_mfma_scale_f32_32x32x64_f8f6f4 v[50:65], v[154:161], v[186:193], v[50:65], v233, v234 op_sel_hi:[0,0,0]
	v_mfma_scale_f32_32x32x64_f8f6f4 v[18:33], v[154:161], v[198:205], v[18:33], v233, v234 op_sel_hi:[0,0,0]
	v_mfma_scale_f32_32x32x64_f8f6f4 v[50:65], v[162:169], v[206:213], v[50:65], v233, v234 op_sel_hi:[0,0,0]
	v_mfma_scale_f32_32x32x64_f8f6f4 v[18:33], v[162:169], v[214:221], v[18:33], v233, v234 op_sel_hi:[0,0,0]
	s_setprio 0
	s_setprio 1
	v_mfma_scale_f32_32x32x64_f8f6f4 v[34:49], v[170:177], v[186:193], v[34:49], v233, v234 op_sel_hi:[0,0,0]
	v_mfma_scale_f32_32x32x64_f8f6f4 v[2:17], v[170:177], v[198:205], v[2:17], v233, v234 op_sel_hi:[0,0,0]
	v_mfma_scale_f32_32x32x64_f8f6f4 v[34:49], v[178:185], v[206:213], v[34:49], v233, v234 op_sel_hi:[0,0,0]
	v_mfma_scale_f32_32x32x64_f8f6f4 v[2:17], v[178:185], v[214:221], v[2:17], v233, v234 op_sel_hi:[0,0,0]
	s_setprio 0
	s_barrier
; #define PG8_STAGE(bufoff, gbase, voff) do { _Pragma("unroll") for (int _i = 0; _i < 2; ++_i) \
;         __builtin_amdgcn_global_load_lds((const unsigned*)((const char*)(gbase) + (voff)[_i]), (PG8_LAS unsigned*)(lds + (bufoff) + ldsw + _i * 8192), 16, 0, 0); } while (0)
; #define PG8_LDA(dst, b, h) do { _Pragma("unroll") for (int m = 0; m < 4; ++m) _Pragma("unroll") for (int k = 0; k < 2; ++k) dst[m][k] = *(const PG8_LAS bf16x8*)(lds + PG8_SA(b, h) + aoff + m * 2048 + k * 1024); } while (0)
; #define PG8_LDB(dst, b, h) do { _Pragma("unroll") for (int n = 0; n < 2; ++n) _Pragma("unroll") for (int k = 0; k < 2; ++k) dst[n][k] = *(const PG8_LAS bf16x8*)(lds + PG8_SB(b, h) + boff + n * 2048 + k * 1024); } while (0)
; #define PG8_MMA(ai, bj, At, Bt) do { __builtin_amdgcn_s_setprio(1); _Pragma("unroll") for (int m = 0; m < 4; ++m) _Pragma("unroll") for (int n = 0; n < 2; ++n) _Pragma("unroll") for (int k = 0; k < 2; ++k) \
;         acc[ai][bj][m][n] = __builtin_amdgcn_mfma_f32_16x16x32_bf16(Bt[n][k], At[m][k], acc[ai][bj][m][n], 0, 0, 0); __builtin_amdgcn_s_setprio(0); } while (0)
; #define PG8_WAIT_V(n) asm volatile("s_waitcnt vmcnt(" #n ")" ::: "memory")
; #define PG8_WAIT_L(n) asm volatile("s_waitcnt lgkmcnt(" #n ")" ::: "memory")
; #define PG8_BAR __builtin_amdgcn_s_barrier()
; #define PG8_SCHED __builtin_amdgcn_sched_barrier(0)
; #define PG8_STAGE(bufoff, gbase, voff) do { _Pragma("unroll") for (int _i = 0; _i < 2; ++_i) \
;         __builtin_amdgcn_global_load_lds((const unsigned*)((const char*)(gbase) + (voff)[_i]), (PG8_LAS unsigned*)(lds + (bufoff) + ldsw + _i * 8192), 16, 0, 0); } while (0)
; template <class Epi, class Sched, int SCW, int SCX, int SCW1 = SCW>
; __device__ __forceinline__ void gemm_phase_f8(PG8_LAS unsigned char* lds, const Gemm g, const Sched& S, const Epi& E, const int tid) {
;     ...
;             PG8_LDB(B0, 1, 0); PG8_LDB(B1, 1, 1); PG8_SCHED; PG8_LDA(At, 1, 0); PG8_STAGE(PG8_SA(0, 1), a2 + hstep, voffA);
;             PG8_WAIT_V(8); PG8_WAIT_L(0); PG8_BAR; PG8_MMA(0, 0, At, B0); PG8_MMA(0, 1, At, B1); PG8_BAR; PG8_SCHED;
;             PG8_LDA(At, 1, 1); PG8_STAGE(PG8_SB(1, 0), b3, voffB); PG8_STAGE(PG8_SB(1, 1), b3 + hstepB, voffB); PG8_STAGE(PG8_SA(1, 0), a3, voffA);
;             PG8_WAIT_V(8); PG8_WAIT_L(0); PG8_BAR; PG8_MMA(1, 0, At, B0); PG8_MMA(1, 1, At, B1); PG8_BAR; PG8_SCHED;
;         }
	s_add_i32 s66, 0, 0x18000
	v_add_u32_e32 v153, s66, v131
	v_add_u32_e32 v158, s66, v144
	ds_read_b128 v[154:157], v153
	ds_read_b128 v[158:161], v158
	v_add_u32_e32 v153, s66, v145
	v_add_u32_e32 v166, s66, v146
	s_add_i32 s87, 0, 0x1c000
	ds_read_b128 v[162:165], v153
	ds_read_b128 v[166:169], v166
	v_add_u32_e32 v153, s87, v131
	v_add_u32_e32 v174, s87, v144
	ds_read_b128 v[170:173], v153
	ds_read_b128 v[174:177], v174
	v_add_u32_e32 v153, s87, v145
	v_add_u32_e32 v182, s87, v146
	ds_read_b128 v[178:181], v153
	ds_read_b128 v[182:185], v182
	s_add_u32 s30, s30, 0x4000
	s_addc_u32 s31, s31, 0
	s_mov_b32 m0, s53
	v_lshl_add_u64 v[224:225], s[30:31], 0, v[132:133]
	ds_read_b128 v[186:189], v149 offset:32768
	ds_read_b128 v[198:201], v149 offset:36864
	ds_read_b128 v[190:193], v150 offset:32768
	ds_read_b128 v[202:205], v150 offset:36864
	ds_read_b128 v[206:209], v151 offset:32768
	ds_read_b128 v[214:217], v151 offset:36864
	ds_read_b128 v[210:213], v152 offset:32768
	ds_read_b128 v[218:221], v152 offset:36864
	global_load_lds_dwordx4 v[224:225], off
	v_lshl_add_u64 v[224:225], s[30:31], 0, v[136:137]
	s_mov_b32 m0, s54
	s_nop 0
	global_load_lds_dwordx4 v[224:225], off
	s_waitcnt vmcnt(8)
	s_waitcnt lgkmcnt(0)
	s_barrier
	s_setprio 1
	s_waitcnt lgkmcnt(0)
	v_mfma_scale_f32_32x32x64_f8f6f4 v[114:129], v[154:161], v[186:193], v[114:129], v233, v234 op_sel_hi:[0,0,0]
	v_mfma_scale_f32_32x32x64_f8f6f4 v[82:97], v[154:161], v[198:205], v[82:97], v233, v234 op_sel_hi:[0,0,0]
	v_mfma_scale_f32_32x32x64_f8f6f4 v[114:129], v[162:169], v[206:213], v[114:129], v233, v234 op_sel_hi:[0,0,0]
	v_mfma_scale_f32_32x32x64_f8f6f4 v[82:97], v[162:169], v[214:221], v[82:97], v233, v234 op_sel_hi:[0,0,0]
	s_setprio 0
	s_setprio 1
	v_mfma_scale_f32_32x32x64_f8f6f4 v[98:113], v[170:177], v[186:193], v[98:113], v233, v234 op_sel_hi:[0,0,0]
	v_mfma_scale_f32_32x32x64_f8f6f4 v[66:81], v[170:177], v[198:205], v[66:81], v233, v234 op_sel_hi:[0,0,0]
	v_mfma_scale_f32_32x32x64_f8f6f4 v[98:113], v[178:185], v[206:213], v[98:113], v233, v234 op_sel_hi:[0,0,0]
	v_mfma_scale_f32_32x32x64_f8f6f4 v[66:81], v[178:185], v[214:221], v[66:81], v233, v234 op_sel_hi:[0,0,0]
	s_setprio 0
	s_barrier
	s_add_u32 s30, s6, 0x8000
	s_addc_u32 s31, s7, 0
	s_add_i32 s66, s66, s50
	v_lshl_add_u64 v[224:225], s[30:31], 0, v[134:135]
	s_mov_b32 m0, s66
	ds_read_b128 v[186:189], v149 offset:49152
	ds_read_b128 v[198:201], v149 offset:53248
	ds_read_b128 v[190:193], v150 offset:49152
	ds_read_b128 v[202:205], v150 offset:53248
	ds_read_b128 v[206:209], v151 offset:49152
	ds_read_b128 v[214:217], v151 offset:53248
	ds_read_b128 v[210:213], v152 offset:49152
	ds_read_b128 v[218:221], v152 offset:53248
	global_load_lds_dwordx4 v[224:225], off nt
	s_add_i32 m0, s66, 0x2000
	s_add_u32 s6, s6, 0xc000
	v_lshl_add_u64 v[224:225], s[30:31], 0, v[138:139]
	s_addc_u32 s7, s7, 0
	s_add_i32 s30, s87, s50
	global_load_lds_dwordx4 v[224:225], off nt
	v_lshl_add_u64 v[224:225], s[6:7], 0, v[134:135]
	s_mov_b32 m0, s30
	v_lshl_add_u64 v[194:195], v[194:195], 0, s[100:101]
	global_load_lds_dwordx4 v[224:225], off nt
	v_lshl_add_u64 v[224:225], s[6:7], 0, v[138:139]
	s_add_i32 m0, s30, 0x2000
	s_nop 0
	global_load_lds_dwordx4 v[224:225], off nt
	s_mov_b32 m0, s59
	s_nop 0
	global_load_lds_dwordx4 v[194:195], off
	v_lshl_add_u64 v[194:195], v[222:223], 0, s[100:101]
	s_mov_b32 m0, s60
	s_nop 0
	global_load_lds_dwordx4 v[194:195], off
	s_waitcnt vmcnt(8)
	s_waitcnt lgkmcnt(0)
	s_barrier
	s_setprio 1
	s_waitcnt lgkmcnt(0)
	v_mfma_scale_f32_32x32x64_f8f6f4 v[50:65], v[154:161], v[186:193], v[50:65], v233, v234 op_sel_hi:[0,0,0]
	v_mfma_scale_f32_32x32x64_f8f6f4 v[18:33], v[154:161], v[198:205], v[18:33], v233, v234 op_sel_hi:[0,0,0]
	v_mfma_scale_f32_32x32x64_f8f6f4 v[50:65], v[162:169], v[206:213], v[50:65], v233, v234 op_sel_hi:[0,0,0]
	v_mfma_scale_f32_32x32x64_f8f6f4 v[18:33], v[162:169], v[214:221], v[18:33], v233, v234 op_sel_hi:[0,0,0]
	s_setprio 0
	s_setprio 1
	v_mfma_scale_f32_32x32x64_f8f6f4 v[34:49], v[170:177], v[186:193], v[34:49], v233, v234 op_sel_hi:[0,0,0]
	v_mfma_scale_f32_32x32x64_f8f6f4 v[2:17], v[170:177], v[198:205], v[2:17], v233, v234 op_sel_hi:[0,0,0]
	v_mfma_scale_f32_32x32x64_f8f6f4 v[34:49], v[178:185], v[206:213], v[34:49], v233, v234 op_sel_hi:[0,0,0]
	v_mfma_scale_f32_32x32x64_f8f6f4 v[2:17], v[178:185], v[214:221], v[2:17], v233, v234 op_sel_hi:[0,0,0]
	s_setprio 0
	s_barrier
	s_add_u32 s13, s13, 0x10000
	s_addc_u32 s17, s17, 0
	s_add_u32 s28, s28, 0x10000
	s_addc_u32 s29, s29, 0
	s_cmp_ge_i32 s63, s24
	s_mov_b32 s6, s63
	s_cbranch_scc0 .LBB0_2000
	s_and_b64 vcc, exec, s[8:9]
	s_cbranch_vccz .LBB0_2003
	s_barrier
